# context-query attention units use the same hand-scheduled tile loop
# speedup vs baseline: 1.0045x; 1.0044x over previous
.LBB0_745:
	s_and_b64 vcc, exec, s[0:1]
	s_cbranch_vccz .LBB0_454
	s_ashr_i32 s0, s22, 2
	s_lshl_b32 s15, s0, 8
	s_lshl_b32 s12, s0, 12
	s_lshl_b32 s0, s22, 7
	v_mov_b32_e32 v205, v3
	v_readlane_b32 s1, v254, 27
	s_and_b32 s8, s0, 0x180
	v_mbcnt_lo_u32_b32 v0, -1, 0
	v_mbcnt_hi_u32_b32 v0, -1, v0
	s_add_i32 s9, s15, 0x4000
	v_add_u32_e32 v204, s1, v0
	s_lshl_b32 s80, s8, 1
	s_add_u32 s0, s52, s80
	v_lshlrev_b32_e32 v0, 4, v204
	v_add_u32_e32 v6, 0x200, v204
	v_add_u32_e32 v12, 0x400, v204
	v_add_u32_e32 v14, 0x600, v204
	v_add_u32_e32 v20, 0x800, v204
	v_add_u32_e32 v22, 0xa00, v204
	v_add_u32_e32 v28, 0xc00, v204
	v_add_u32_e32 v32, 0xe00, v204
	s_addc_u32 s1, s53, 0
	v_and_b32_e32 v2, 0xf0, v0
	v_ashrrev_i32_e32 v36, 4, v204
	v_ashrrev_i32_e32 v38, 4, v6
	v_ashrrev_i32_e32 v40, 4, v12
	v_ashrrev_i32_e32 v42, 4, v14
	v_ashrrev_i32_e32 v44, 4, v20
	v_ashrrev_i32_e32 v46, 4, v22
	v_ashrrev_i32_e32 v48, 4, v28
	v_ashrrev_i32_e32 v50, 4, v32
	v_lshl_add_u64 v[0:1], s[0:1], 0, v[2:3]
	v_add_u32_e32 v4, s9, v36
	s_movk_i32 s13, 0x1400
	v_add_u32_e32 v6, s9, v38
	v_add_u32_e32 v12, s9, v40
	v_add_u32_e32 v14, s9, v42
	v_add_u32_e32 v20, s9, v44
	v_add_u32_e32 v22, s9, v46
	v_add_u32_e32 v28, s9, v48
	v_add_u32_e32 v32, s9, v50
	v_mad_i64_i32 v[4:5], s[2:3], v4, s13, v[0:1]
	v_mad_i64_i32 v[8:9], s[2:3], v6, s13, v[0:1]
	v_mad_i64_i32 v[12:13], s[2:3], v12, s13, v[0:1]
	v_mad_i64_i32 v[16:17], s[2:3], v14, s13, v[0:1]
	v_mad_i64_i32 v[20:21], s[2:3], v20, s13, v[0:1]
	v_mad_i64_i32 v[24:25], s[2:3], v22, s13, v[0:1]
	v_mad_i64_i32 v[28:29], s[2:3], v28, s13, v[0:1]
	v_mad_i64_i32 v[0:1], s[2:3], v32, s13, v[0:1]
	global_load_dwordx4 v[4:7], v[4:5], off
	s_nop 0
	global_load_dwordx4 v[8:11], v[8:9], off
	s_nop 0
	global_load_dwordx4 v[12:15], v[12:13], off
	s_nop 0
	global_load_dwordx4 v[16:19], v[16:17], off
	s_nop 0
	global_load_dwordx4 v[20:23], v[20:21], off
	s_nop 0
	global_load_dwordx4 v[24:27], v[24:25], off
	v_add_u32_e32 v206, 0x11800, v205
	global_load_dwordx4 v[28:31], v[28:29], off
	v_ashrrev_i32_e32 v51, 6, v204
	global_load_dwordx4 v[32:35], v[0:1], off
	v_add_u32_e32 v0, v206, v2
	v_mad_u64_u32 v[36:37], s[10:11], v36, s30, v[0:1]
	v_mad_u64_u32 v[38:39], s[10:11], v38, s30, v[0:1]
	v_mad_u64_u32 v[40:41], s[10:11], v40, s30, v[0:1]
	v_mad_u64_u32 v[42:43], s[10:11], v42, s30, v[0:1]
	v_mad_u64_u32 v[44:45], s[10:11], v44, s30, v[0:1]
	v_mad_u64_u32 v[46:47], s[10:11], v46, s30, v[0:1]
	v_mad_u64_u32 v[48:49], s[10:11], v48, s30, v[0:1]
	v_mad_u64_u32 v[0:1], s[10:11], v50, s30, v[0:1]
	v_and_b32_e32 v2, 63, v204
	v_readfirstlane_b32 s2, v51
	s_mov_b64 s[24:25], 0x400
	v_mov_b32_e32 v226, 0x3ecc95a3
	v_mov_b32_e32 v210, 0
	v_mov_b32_e32 v208, 0xf149f2ca
	s_waitcnt vmcnt(7)
	ds_write_b128 v36, v[4:7]
	s_waitcnt vmcnt(6)
	ds_write_b128 v38, v[8:11]
	s_waitcnt vmcnt(5)
	ds_write_b128 v40, v[12:15]
	s_waitcnt vmcnt(4)
	ds_write_b128 v42, v[16:19]
	s_waitcnt vmcnt(3)
	ds_write_b128 v44, v[20:23]
	s_waitcnt vmcnt(2)
	ds_write_b128 v46, v[24:27]
	s_waitcnt vmcnt(1)
	ds_write_b128 v48, v[28:31]
	v_or_b32_e32 v4, s9, v2
	v_lshlrev_b32_e32 v2, 2, v2
	v_mov_b32_e32 v14, v3
	s_waitcnt vmcnt(0)
	ds_write_b128 v0, v[32:35]
	v_mov_b64_e32 v[0:1], s[52:53]
	v_mad_i64_i32 v[0:1], s[10:11], v4, s13, v[0:1]
	s_lshl_b32 s10, s2, 3
	s_add_i32 s11, s12, 0xffffff00
	s_cmp_lt_i32 s2, 32
	s_cselect_b32 s3, s9, s11
	s_add_i32 s3, s3, s10
	s_mul_hi_i32 s12, s3, 0x1400
	s_mulk_i32 s3, 0x1400
	s_add_u32 s3, s52, s3
	v_lshlrev_b32_e32 v4, 3, v51
	s_addc_u32 s13, s53, s12
	v_lshl_add_u64 v[0:1], v[0:1], 0, s[80:81]
	v_ashrrev_i32_e32 v5, 31, v4
	s_add_u32 s12, s3, s80
	v_lshl_add_u64 v[0:1], v[4:5], 1, v[0:1]
	s_addc_u32 s13, s13, 0
	global_load_dwordx4 v[176:179], v[0:1], off offset:2048
	global_load_dwordx4 v[180:183], v[0:1], off offset:2176
	v_lshl_add_u64 v[0:1], s[12:13], 0, v[2:3]
	s_mul_i32 s13, s2, 0x880
	v_add_u32_e32 v4, s13, v205
	s_or_b32 s14, s10, 1
	v_readfirstlane_b32 s3, v4
	s_cmpk_lt_i32 s14, 0x100
	s_mov_b32 m0, s3
	s_cselect_b32 s3, s9, s11
	s_add_i32 s3, s3, s14
	s_mul_hi_i32 s12, s3, 0x1400
	s_mulk_i32 s3, 0x1400
	s_add_u32 s3, s52, s3
	s_mulk_i32 s14, 0x110
	s_addc_u32 s12, s53, s12
	v_add_u32_e32 v4, s14, v205
	v_lshl_add_u64 v[0:1], v[0:1], 0, s[24:25]
	s_add_u32 s22, s3, s80
	v_readfirstlane_b32 s3, v4
	global_load_lds_dword v[0:1], off
	s_addc_u32 s23, s12, 0
	s_mov_b32 m0, s3
	s_or_b32 s3, s10, 2
	s_cmpk_lt_i32 s3, 0x100
	s_cselect_b32 s12, s9, s11
	s_add_i32 s3, s12, s3
	s_mul_hi_i32 s12, s3, 0x1400
	s_mulk_i32 s3, 0x1400
	s_add_u32 s3, s52, s3
	s_addc_u32 s12, s53, s12
	v_lshl_add_u64 v[0:1], s[22:23], 0, v[2:3]
	s_add_u32 s22, s3, s80
	s_addc_u32 s23, s12, 0
	s_add_i32 s3, s14, 0x110
	v_add_u32_e32 v4, s3, v205
	v_lshl_add_u64 v[0:1], v[0:1], 0, s[24:25]
	v_readfirstlane_b32 s3, v4
	global_load_lds_dword v[0:1], off
	s_mov_b32 m0, s3
	s_or_b32 s3, s10, 3
	s_cmpk_lt_i32 s3, 0x100
	s_cselect_b32 s12, s9, s11
	s_add_i32 s3, s12, s3
	s_mul_hi_i32 s12, s3, 0x1400
	s_mulk_i32 s3, 0x1400
	s_add_u32 s3, s52, s3
	s_addc_u32 s12, s53, s12
	v_lshl_add_u64 v[0:1], s[22:23], 0, v[2:3]
	s_add_u32 s22, s3, s80
	s_addc_u32 s23, s12, 0
	s_add_i32 s3, s14, 0x220
	v_add_u32_e32 v4, s3, v205
	v_lshl_add_u64 v[0:1], v[0:1], 0, s[24:25]
	v_readfirstlane_b32 s3, v4
	global_load_lds_dword v[0:1], off
	s_mov_b32 m0, s3
	s_or_b32 s3, s10, 4
	s_cmpk_lt_i32 s3, 0x100
	s_cselect_b32 s12, s9, s11
	s_add_i32 s3, s12, s3
	s_mul_hi_i32 s12, s3, 0x1400
	s_mulk_i32 s3, 0x1400
	s_add_u32 s3, s52, s3
	s_addc_u32 s12, s53, s12
	v_lshl_add_u64 v[0:1], s[22:23], 0, v[2:3]
	s_add_u32 s22, s3, s80
	s_addc_u32 s23, s12, 0
	s_add_i32 s3, s14, 0x330
	v_add_u32_e32 v4, s3, v205
	v_lshl_add_u64 v[0:1], v[0:1], 0, s[24:25]
	v_readfirstlane_b32 s3, v4
	global_load_lds_dword v[0:1], off
	s_mov_b32 m0, s3
	s_or_b32 s3, s10, 5
	s_cmpk_lt_i32 s3, 0x100
	s_cselect_b32 s12, s9, s11
	s_add_i32 s3, s12, s3
	s_mul_hi_i32 s12, s3, 0x1400
	s_mulk_i32 s3, 0x1400
	s_add_u32 s3, s52, s3
	s_addc_u32 s12, s53, s12
	v_lshl_add_u64 v[0:1], s[22:23], 0, v[2:3]
	s_add_u32 s22, s3, s80
	s_addc_u32 s23, s12, 0
	s_add_i32 s3, s14, 0x440
	v_add_u32_e32 v4, s3, v205
	v_lshl_add_u64 v[0:1], v[0:1], 0, s[24:25]
	v_readfirstlane_b32 s3, v4
	global_load_lds_dword v[0:1], off
	s_mov_b32 m0, s3
	s_or_b32 s3, s10, 6
	s_cmpk_lt_i32 s3, 0x100
	s_cselect_b32 s12, s9, s11
	s_add_i32 s3, s12, s3
	s_mul_hi_i32 s12, s3, 0x1400
	s_mulk_i32 s3, 0x1400
	s_add_u32 s3, s52, s3
	s_addc_u32 s12, s53, s12
	v_lshl_add_u64 v[0:1], s[22:23], 0, v[2:3]
	s_add_u32 s22, s3, s80
	s_addc_u32 s23, s12, 0
	s_add_i32 s3, s14, 0x550
	v_add_u32_e32 v4, s3, v205
	v_lshl_add_u64 v[0:1], v[0:1], 0, s[24:25]
	v_readfirstlane_b32 s3, v4
	global_load_lds_dword v[0:1], off
	s_mov_b32 m0, s3
	s_or_b32 s3, s10, 7
	s_cmpk_lt_i32 s3, 0x100
	s_cselect_b32 s12, s9, s11
	s_add_i32 s3, s12, s3
	s_mul_hi_i32 s12, s3, 0x1400
	s_mulk_i32 s3, 0x1400
	s_add_u32 s3, s52, s3
	s_addc_u32 s12, s53, s12
	v_lshl_add_u64 v[0:1], s[22:23], 0, v[2:3]
	s_add_u32 s22, s3, s80
	v_lshl_add_u64 v[0:1], v[0:1], 0, s[24:25]
	s_addc_u32 s23, s12, 0
	s_add_i32 s3, s14, 0x660
	global_load_lds_dword v[0:1], off
	v_lshl_add_u64 v[0:1], s[22:23], 0, v[2:3]
	v_add_u32_e32 v2, s3, v205
	v_lshl_add_u64 v[0:1], v[0:1], 0, s[24:25]
	v_readfirstlane_b32 s3, v2
	s_mov_b32 m0, s3
	s_movk_i32 s3, 0x480
	global_load_lds_dword v[0:1], off
	v_bfe_u32 v0, v204, 2, 2
	v_and_b32_e32 v1, 12, v204
	v_cmp_ne_u32_e32 vcc, 2, v0
	v_mov_b32_e32 v15, v3
	v_mov_b32_e32 v2, v3
	v_cndmask_b32_e32 v1, 4, v1, vcc
	v_cmp_ne_u32_e32 vcc, 1, v0
	v_mov_b32_e32 v4, v3
	v_mov_b32_e32 v5, v3
	v_cndmask_b32_e32 v0, 8, v1, vcc
	v_and_or_b32 v0, v204, 51, v0
	v_mul_lo_u32 v1, v51, s3
	v_lshlrev_b32_e32 v0, 1, v0
	v_add3_u32 v0, v205, v1, v0
	s_waitcnt vmcnt(0)
	ds_write_b16 v0, v176 offset:34816
	ds_write_b16_d16_hi v0, v176 offset:34960
	ds_write_b16 v0, v177 offset:35104
	ds_write_b16_d16_hi v0, v177 offset:35248
	ds_write_b16 v0, v178 offset:35392
	ds_write_b16_d16_hi v0, v178 offset:35536
	ds_write_b16 v0, v179 offset:35680
	ds_write_b16_d16_hi v0, v179 offset:35824
	ds_write_b16 v0, v180 offset:44032
	ds_write_b16_d16_hi v0, v180 offset:44176
	ds_write_b16 v0, v181 offset:44320
	ds_write_b16_d16_hi v0, v181 offset:44464
	ds_write_b16 v0, v182 offset:44608
	ds_write_b16_d16_hi v0, v182 offset:44752
	ds_write_b16 v0, v183 offset:44896
	ds_write_b16_d16_hi v0, v183 offset:45040
	v_mov_b32_e32 v0, v3
	v_mov_b32_e32 v1, v3
	v_mov_b32_e32 v6, v3
	v_mov_b32_e32 v7, v3
	v_mov_b32_e32 v8, v3
	v_mov_b32_e32 v9, v3
	v_mov_b32_e32 v10, v3
	v_mov_b32_e32 v11, v3
	v_mov_b32_e32 v12, v3
	v_mov_b32_e32 v13, v3
	v_mov_b64_e32 v[30:31], v[14:15]
	v_mov_b64_e32 v[62:63], v[14:15]
	v_mov_b64_e32 v[94:95], v[14:15]
	v_mov_b64_e32 v[126:127], v[14:15]
	v_mov_b64_e32 v[46:47], v[14:15]
	v_mov_b64_e32 v[78:79], v[14:15]
	v_mov_b64_e32 v[110:111], v[14:15]
	v_mov_b64_e32 v[142:143], v[14:15]
	s_lshl_b32 s12, s2, 5
	s_addk_i32 s15, 0x4040
	s_mov_b32 s22, 0
	v_mov_b64_e32 v[28:29], v[12:13]
	v_mov_b64_e32 v[26:27], v[10:11]
	v_mov_b64_e32 v[24:25], v[8:9]
	v_mov_b64_e32 v[22:23], v[6:7]
	v_mov_b64_e32 v[20:21], v[4:5]
	v_mov_b64_e32 v[18:19], v[2:3]
	v_mov_b64_e32 v[16:17], v[0:1]
	v_mov_b64_e32 v[60:61], v[12:13]
	v_mov_b64_e32 v[58:59], v[10:11]
	v_mov_b64_e32 v[56:57], v[8:9]
	v_mov_b64_e32 v[54:55], v[6:7]
	v_mov_b64_e32 v[52:53], v[4:5]
	v_mov_b64_e32 v[50:51], v[2:3]
	v_mov_b64_e32 v[48:49], v[0:1]
	v_mov_b64_e32 v[92:93], v[12:13]
	v_mov_b64_e32 v[90:91], v[10:11]
	v_mov_b64_e32 v[88:89], v[8:9]
	v_mov_b64_e32 v[86:87], v[6:7]
	v_mov_b64_e32 v[84:85], v[4:5]
	v_mov_b64_e32 v[82:83], v[2:3]
	v_mov_b64_e32 v[80:81], v[0:1]
	v_mov_b64_e32 v[124:125], v[12:13]
	v_mov_b64_e32 v[122:123], v[10:11]
	v_mov_b64_e32 v[120:121], v[8:9]
	v_mov_b64_e32 v[118:119], v[6:7]
	v_mov_b64_e32 v[116:117], v[4:5]
	v_mov_b64_e32 v[114:115], v[2:3]
	v_mov_b64_e32 v[112:113], v[0:1]
	v_mov_b64_e32 v[44:45], v[12:13]
	v_mov_b64_e32 v[42:43], v[10:11]
	v_mov_b64_e32 v[40:41], v[8:9]
	v_mov_b64_e32 v[38:39], v[6:7]
	v_mov_b64_e32 v[36:37], v[4:5]
	v_mov_b64_e32 v[34:35], v[2:3]
	v_mov_b64_e32 v[32:33], v[0:1]
	v_mov_b64_e32 v[76:77], v[12:13]
	v_mov_b64_e32 v[74:75], v[10:11]
	v_mov_b64_e32 v[72:73], v[8:9]
	v_mov_b64_e32 v[70:71], v[6:7]
	v_mov_b64_e32 v[68:69], v[4:5]
	v_mov_b64_e32 v[66:67], v[2:3]
	v_mov_b64_e32 v[64:65], v[0:1]
	v_mov_b64_e32 v[108:109], v[12:13]
	v_mov_b64_e32 v[106:107], v[10:11]
	v_mov_b64_e32 v[104:105], v[8:9]
	v_mov_b64_e32 v[102:103], v[6:7]
	v_mov_b64_e32 v[100:101], v[4:5]
	v_mov_b64_e32 v[98:99], v[2:3]
	v_mov_b64_e32 v[96:97], v[0:1]
	v_mov_b64_e32 v[140:141], v[12:13]
	v_mov_b64_e32 v[138:139], v[10:11]
	v_mov_b64_e32 v[136:137], v[8:9]
	v_mov_b64_e32 v[134:135], v[6:7]
	v_mov_b64_e32 v[132:133], v[4:5]
	v_mov_b64_e32 v[130:131], v[2:3]
	v_mov_b64_e32 v[128:129], v[0:1]
	v_mov_b32_e32 v209, 0xf149f2ca
	v_mov_b32_e32 v207, 0
	s_mov_b32 s25, 0
	s_waitcnt lgkmcnt(0)
	s_barrier
	v_and_b32_e32 v2, 31, v204
	v_bfe_u32 v15, v204, 5, 1
	v_lshlrev_b32_e32 v15, 4, v15
	v_or_b32_e32 v13, s12, v2
	v_mul_u32_u24_e32 v1, 0x90, v2
	v_mad_u32_u24 v0, v2, s30, v15
	v_mul_lo_u32 v13, v13, s30
	v_add_u32_e32 v0, v0, v205
	v_add3_u32 v1, v1, v15, v205
	v_add3_u32 v13, v206, v13, v15
	v_bfe_u32 v15, v204, 2, 2
	v_and_b32_e32 v2, 12, v204
	v_cmp_ne_u32_e32 vcc, 2, v15
	s_movk_i32 s24, 0x480
	v_ashrrev_i32_e32 v211, 6, v204
	v_cndmask_b32_e32 v2, 4, v2, vcc
	v_cmp_ne_u32_e32 vcc, 1, v15
	v_mul_lo_u32 v211, v211, s24
	s_nop 0
	v_cndmask_b32_e32 v15, 8, v2, vcc
	v_and_or_b32 v2, v204, 51, v15
	v_lshlrev_b32_e32 v2, 1, v2
	v_add3_u32 v2, v205, v211, v2
.LBB0_747:
	s_add_i32 s23, s25, 1
	s_and_b32 s27, s25, 1
	s_mul_i32 s26, s27, 0x4400
	s_mul_i32 s31, s27, 0x4800
	v_add_u32_e32 v12, s26, v0
	v_add_u32_e32 v14, s31, v1
	ds_read_b128 v[228:231], v12 offset:0
	ds_read_b128 v[232:235], v12 offset:32
	ds_read_b128 v[236:239], v12 offset:64
	ds_read_b128 v[240:243], v12 offset:96
	ds_read_b128 v[244:247], v13 offset:0
	ds_read_b128 v[248:251], v13 offset:32
	ds_read_b128 v[4:7], v13 offset:64
	ds_read_b128 v[8:11], v13 offset:96
	ds_read_b128 v[184:187], v14 offset:34816
	ds_read_b128 v[188:191], v14 offset:39424
	ds_read_b128 v[192:195], v14 offset:44032
	ds_read_b128 v[196:199], v14 offset:48640
	ds_read_b128 v[200:203], v14 offset:34848
	ds_read_b128 v[212:215], v14 offset:39456
	ds_read_b128 v[216:219], v14 offset:44064
	s_cmp_gt_u32 s25, 2
	s_cbranch_scc1 .Lat2_noload
	s_mov_b32 s26, s15
	s_mov_b32 s31, s9
	s_add_i32 s26, s26, s22
	v_and_b32_e32 v15, 63, v204
	v_ashrrev_i32_e32 v227, 6, v204
	v_add_u32_e32 v211, s26, v15
	v_lshlrev_b32_e32 v227, 4, v227
	s_add_i32 s31, s31, s10
	v_mul_u32_u24_e32 v211, 0x1400, v211
	s_add_i32 s31, s31, s22
	s_add_i32 s31, s31, 64
	v_add_u32_e32 v211, v211, v227
	s_mul_hi_i32 s37, s31, 0x1400
	s_mul_i32 s36, s31, 0x1400
	v_lshlrev_b32_e32 v15, 2, v15
	global_load_dwordx4 v[176:179], v211, s[0:1] offset:2048
	global_load_dwordx4 v[180:183], v211, s[0:1] offset:2176
	s_add_u32 s36, s0, s36
	s_addc_u32 s37, s1, s37
	v_readfirstlane_b32 s2, v205
	s_xor_b32 s3, s27, 1
	v_add_u32_e32 v15, 0x400, v15
	s_mul_i32 s3, s3, 0x4400
	s_add_i32 s2, s2, s13
	s_add_i32 s2, s2, s3
	s_add_i32 m0, s2, 0
	s_nop 0
	global_load_lds_dword v15, s[36:37]
	s_add_u32 s36, s36, 0x1400
	s_addc_u32 s37, s37, 0
	s_add_i32 m0, s2, 272
	s_nop 0
	global_load_lds_dword v15, s[36:37]
	s_add_u32 s36, s36, 0x1400
	s_addc_u32 s37, s37, 0
	s_add_i32 m0, s2, 544
	s_nop 0
	global_load_lds_dword v15, s[36:37]
	s_add_u32 s36, s36, 0x1400
	s_addc_u32 s37, s37, 0
	s_add_i32 m0, s2, 816
	s_nop 0
	global_load_lds_dword v15, s[36:37]
	s_add_u32 s36, s36, 0x1400
	s_addc_u32 s37, s37, 0
	s_add_i32 m0, s2, 1088
	s_nop 0
	global_load_lds_dword v15, s[36:37]
	s_add_u32 s36, s36, 0x1400
	s_addc_u32 s37, s37, 0
	s_add_i32 m0, s2, 1360
	s_nop 0
	global_load_lds_dword v15, s[36:37]
	s_add_u32 s36, s36, 0x1400
	s_addc_u32 s37, s37, 0
	s_add_i32 m0, s2, 1632
	s_nop 0
	global_load_lds_dword v15, s[36:37]
	s_add_u32 s36, s36, 0x1400
	s_addc_u32 s37, s37, 0
	s_add_i32 m0, s2, 1904
	s_nop 0
	global_load_lds_dword v15, s[36:37]

.Lat2_back1_s1:
	v_sub_f32_e32 v160, v160, v208
	v_sub_f32_e32 v161, v161, v208
	v_mfma_f32_32x32x16_bf16 v[96:111], v[188:191], v[144:147], v[96:111]
	v_sub_f32_e32 v162, v162, v208
	v_sub_f32_e32 v163, v163, v208
	v_exp_f32_e32 v160, v160
	v_exp_f32_e32 v161, v161
	v_exp_f32_e32 v162, v162
	v_exp_f32_e32 v163, v163
	v_mfma_f32_32x32x16_bf16 v[64:79], v[192:195], v[144:147], v[64:79]
	v_sub_f32_e32 v164, v164, v208
	v_sub_f32_e32 v165, v165, v208
	v_sub_f32_e32 v166, v166, v208
	v_sub_f32_e32 v167, v167, v208
	v_exp_f32_e32 v164, v164
	v_exp_f32_e32 v165, v165
	v_exp_f32_e32 v166, v166
	v_mfma_f32_32x32x16_bf16 v[32:47], v[196:199], v[144:147], v[32:47]
	v_exp_f32_e32 v167, v167
	v_sub_f32_e32 v168, v168, v208
	v_sub_f32_e32 v169, v169, v208
	v_sub_f32_e32 v170, v170, v208
	v_sub_f32_e32 v171, v171, v208
	v_exp_f32_e32 v168, v168
	v_exp_f32_e32 v169, v169
	v_exp_f32_e32 v170, v170
	v_mfma_f32_32x32x16_bf16 v[128:143], v[200:203], v[148:151], v[128:143]
	v_exp_f32_e32 v171, v171
	v_sub_f32_e32 v172, v172, v208
	v_sub_f32_e32 v173, v173, v208
	v_sub_f32_e32 v174, v174, v208
	v_sub_f32_e32 v175, v175, v208
	v_exp_f32_e32 v172, v172
	v_exp_f32_e32 v173, v173
	v_mfma_f32_32x32x16_bf16 v[96:111], v[212:215], v[148:151], v[96:111]
	v_exp_f32_e32 v174, v174
	v_exp_f32_e32 v175, v175
	v_add_f32_e32 v15, v160, v161
	v_add_f32_e32 v211, v162, v163
	v_add_f32_e32 v15, v15, v211
	v_add_f32_e32 v211, v164, v165
	v_add_f32_e32 v224, v166, v167
	v_add_f32_e32 v211, v211, v224
	v_add_f32_e32 v224, v168, v169
	v_mfma_f32_32x32x16_bf16 v[64:79], v[216:219], v[148:151], v[64:79]
	v_add_f32_e32 v225, v170, v171
	v_add_f32_e32 v224, v224, v225
	v_add_f32_e32 v225, v172, v173
	v_add_f32_e32 v227, v174, v175
	v_add_f32_e32 v225, v225, v227
	v_add_f32_e32 v15, v15, v211
	v_add_f32_e32 v224, v224, v225
	v_add_f32_e32 v15, v15, v224
	v_add_f32_e32 v207, v207, v15
	v_cvt_pk_bf16_f32 v160, v160, v161
	v_cvt_pk_bf16_f32 v161, v162, v163
	v_cvt_pk_bf16_f32 v162, v164, v165
	v_cvt_pk_bf16_f32 v163, v166, v167
	v_cvt_pk_bf16_f32 v164, v168, v169
	v_cvt_pk_bf16_f32 v165, v170, v171
	v_cvt_pk_bf16_f32 v166, v172, v173
	v_cvt_pk_bf16_f32 v167, v174, v175
	v_mfma_f32_32x32x16_bf16 v[32:47], v[220:223], v[148:151], v[32:47]
	s_nop 1
	v_mfma_f32_32x32x16_bf16 v[112:127], v[184:187], v[160:163], v[112:127]
	s_xor_b32 s24, s27, 1
	s_mulk_i32 s24, 0x4800
	s_waitcnt vmcnt(0)
	v_mfma_f32_32x32x16_bf16 v[80:95], v[188:191], v[160:163], v[80:95]
	v_add_u32_e32 v15, s24, v2
	ds_write_b16 v15, v176 offset:34816
	v_mfma_f32_32x32x16_bf16 v[48:63], v[192:195], v[160:163], v[48:63]
	ds_write_b16_d16_hi v15, v176 offset:34960
	ds_write_b16 v15, v177 offset:35104
	ds_write_b16_d16_hi v15, v177 offset:35248
	v_mfma_f32_32x32x16_bf16 v[16:31], v[196:199], v[160:163], v[16:31]
	ds_write_b16 v15, v178 offset:35392
	ds_write_b16_d16_hi v15, v178 offset:35536
	v_mfma_f32_32x32x16_bf16 v[112:127], v[200:203], v[164:167], v[112:127]
	ds_write_b16 v15, v179 offset:35680
	ds_write_b16_d16_hi v15, v179 offset:35824
	ds_write_b16 v15, v180 offset:44032
	v_mfma_f32_32x32x16_bf16 v[80:95], v[212:215], v[164:167], v[80:95]
	ds_write_b16_d16_hi v15, v180 offset:44176
	ds_write_b16 v15, v181 offset:44320
	v_mfma_f32_32x32x16_bf16 v[48:63], v[216:219], v[164:167], v[48:63]
	ds_write_b16_d16_hi v15, v181 offset:44464
	ds_write_b16 v15, v182 offset:44608
	ds_write_b16_d16_hi v15, v182 offset:44752
	v_mfma_f32_32x32x16_bf16 v[16:31], v[220:223], v[164:167], v[16:31]
	ds_write_b16 v15, v183 offset:44896
	ds_write_b16_d16_hi v15, v183 offset:45040
	s_add_i32 s22, s22, 64
	s_cmpk_lg_i32 s22, 0x100
	s_waitcnt vmcnt(0) lgkmcnt(0)
	s_barrier
	s_cbranch_scc0 .Lat2_exit
	s_mov_b32 s25, s23
	s_branch .LBB0_747
.Lat2_exit:
	s_mov_b32 s25, s27
	s_nop 15
	s_branch .LBB0_453

.Lat2_slow1_s1:
	s_nop 15
	v_max_f32_e32 v211, v208, v15
	v_sub_f32_e32 v224, v208, v211
	v_exp_f32_e32 v224, v224
	v_mov_b32_e32 v208, v211
	s_nop 0
	v_pk_mul_f32 v[112:113], v[112:113], v[224:225] op_sel_hi:[1,0]
	v_pk_mul_f32 v[114:115], v[114:115], v[224:225] op_sel_hi:[1,0]
	v_pk_mul_f32 v[116:117], v[116:117], v[224:225] op_sel_hi:[1,0]
	v_pk_mul_f32 v[118:119], v[118:119], v[224:225] op_sel_hi:[1,0]
	v_pk_mul_f32 v[120:121], v[120:121], v[224:225] op_sel_hi:[1,0]
	v_pk_mul_f32 v[122:123], v[122:123], v[224:225] op_sel_hi:[1,0]
	v_pk_mul_f32 v[124:125], v[124:125], v[224:225] op_sel_hi:[1,0]
	v_pk_mul_f32 v[126:127], v[126:127], v[224:225] op_sel_hi:[1,0]
	v_pk_mul_f32 v[80:81], v[80:81], v[224:225] op_sel_hi:[1,0]
	v_pk_mul_f32 v[82:83], v[82:83], v[224:225] op_sel_hi:[1,0]
	v_pk_mul_f32 v[84:85], v[84:85], v[224:225] op_sel_hi:[1,0]
	v_pk_mul_f32 v[86:87], v[86:87], v[224:225] op_sel_hi:[1,0]
	v_pk_mul_f32 v[88:89], v[88:89], v[224:225] op_sel_hi:[1,0]
	v_pk_mul_f32 v[90:91], v[90:91], v[224:225] op_sel_hi:[1,0]
	v_pk_mul_f32 v[92:93], v[92:93], v[224:225] op_sel_hi:[1,0]
	v_pk_mul_f32 v[94:95], v[94:95], v[224:225] op_sel_hi:[1,0]
	v_pk_mul_f32 v[48:49], v[48:49], v[224:225] op_sel_hi:[1,0]
	v_pk_mul_f32 v[50:51], v[50:51], v[224:225] op_sel_hi:[1,0]
	v_pk_mul_f32 v[52:53], v[52:53], v[224:225] op_sel_hi:[1,0]
	v_pk_mul_f32 v[54:55], v[54:55], v[224:225] op_sel_hi:[1,0]
	v_pk_mul_f32 v[56:57], v[56:57], v[224:225] op_sel_hi:[1,0]
	v_pk_mul_f32 v[58:59], v[58:59], v[224:225] op_sel_hi:[1,0]
	v_pk_mul_f32 v[60:61], v[60:61], v[224:225] op_sel_hi:[1,0]
	v_pk_mul_f32 v[62:63], v[62:63], v[224:225] op_sel_hi:[1,0]
	v_pk_mul_f32 v[16:17], v[16:17], v[224:225] op_sel_hi:[1,0]
	v_pk_mul_f32 v[18:19], v[18:19], v[224:225] op_sel_hi:[1,0]
	v_pk_mul_f32 v[20:21], v[20:21], v[224:225] op_sel_hi:[1,0]
	v_pk_mul_f32 v[22:23], v[22:23], v[224:225] op_sel_hi:[1,0]
	v_pk_mul_f32 v[24:25], v[24:25], v[224:225] op_sel_hi:[1,0]
	v_pk_mul_f32 v[26:27], v[26:27], v[224:225] op_sel_hi:[1,0]
	v_pk_mul_f32 v[28:29], v[28:29], v[224:225] op_sel_hi:[1,0]
	v_pk_mul_f32 v[30:31], v[30:31], v[224:225] op_sel_hi:[1,0]
	v_mul_f32_e32 v207, v207, v224
	s_nop 1
	s_branch .Lat2_back1_s1
.LBB0_761:
	v_readlane_b32 s0, v253, 52
	v_readlane_b32 s1, v253, 53
	s_and_b64 vcc, exec, s[0:1]
	s_cbranch_vccnz .LBB0_808
	v_readlane_b32 s2, v253, 50
	v_readlane_b32 s3, v253, 51
	s_waitcnt vmcnt(0)
	s_waitcnt vmcnt(0)
	s_barrier
	s_mov_b64 s[0:1], exec
	v_readlane_b32 s8, v255, 34
	v_readlane_b32 s9, v255, 35
	s_and_b64 s[8:9], s[0:1], s[8:9]
	s_mov_b64 exec, s[8:9]
	s_cbranch_execz .LBB0_807
	v_readlane_b32 s8, v255, 30
	s_waitcnt vmcnt(0) expcnt(0) lgkmcnt(0)
	s_nop 0
	v_mov_b32_e32 v0, s8
	ds_read_b32 v2, v0
	v_readlane_b32 s8, v255, 31
	s_waitcnt lgkmcnt(0)
	v_cmp_ne_u32_e32 vcc, 0, v2
	v_mov_b32_e32 v0, s8
	ds_read_b32 v0, v0
	s_cbranch_vccnz .LBB0_777
	v_readlane_b32 s8, v253, 0
	v_readlane_b32 s9, v253, 1
	s_load_dwordx2 s[12:13], s[8:9], 0x4
	s_add_u32 s8, s2, 0x1000
	s_addc_u32 s9, s3, 0
	s_add_u32 s10, s2, 0x1100
	s_addc_u32 s11, s3, 0
	s_waitcnt lgkmcnt(0)
	s_mul_i32 s25, s12, s74
	s_add_u32 s12, s2, 0x1200
	s_mul_i32 s25, s25, s13
	s_addc_u32 s13, s3, 0
	s_add_u32 s14, s2, 0x1300
	s_addc_u32 s15, s3, 0
	s_mov_b32 s31, 1
	s_mov_b64 s[16:17], 0
	s_branch .LBB0_767
